# baseline (speedup 1.0000x reference)
.Lk1_nowarm9:
	s_waitcnt vmcnt(49)
	s_cmp_lg_u32 s21, 0
	s_cbranch_scc1 .Lk1_nowarmk
	v_lshlrev_b32_e32 v3, 6, v0
	s_add_u32 s30, s30, 0x1000
	s_addc_u32 s31, s31, 0
	global_load_dword v93, v3, s[30:31]
	s_add_u32 s30, s30, 0x1000
	s_addc_u32 s31, s31, 0
	global_load_dword v94, v3, s[30:31]
	s_and_b32 s30, s0, 0xfffff000
	s_mov_b32 s31, s1
	global_load_dword v95, v3, s[30:31]
.Lk1_nowarmk:
	v_max3_f32 v76, v8, v9, v10
	v_max3_f32 v76, v76, v11, v12
	v_max3_f32 v76, v76, v13, v14
	v_max3_f32 v76, v76, v15, v16
	v_max3_f32 v76, v76, v17, v18
	v_max3_f32 v76, v76, v19, v20
	v_max3_f32 v76, v76, v21, v22
	v_max_f32_e32 v76, v76, v23
	v_pk_add_f32 v[8:9], v[8:9], v[76:77] op_sel_hi:[1,0] neg_lo:[0,1] neg_hi:[0,1]
	v_pk_add_f32 v[10:11], v[10:11], v[76:77] op_sel_hi:[1,0] neg_lo:[0,1] neg_hi:[0,1]
	v_pk_add_f32 v[12:13], v[12:13], v[76:77] op_sel_hi:[1,0] neg_lo:[0,1] neg_hi:[0,1]
	v_pk_add_f32 v[14:15], v[14:15], v[76:77] op_sel_hi:[1,0] neg_lo:[0,1] neg_hi:[0,1]
	v_pk_add_f32 v[16:17], v[16:17], v[76:77] op_sel_hi:[1,0] neg_lo:[0,1] neg_hi:[0,1]
	v_pk_add_f32 v[18:19], v[18:19], v[76:77] op_sel_hi:[1,0] neg_lo:[0,1] neg_hi:[0,1]
	v_pk_add_f32 v[20:21], v[20:21], v[76:77] op_sel_hi:[1,0] neg_lo:[0,1] neg_hi:[0,1]
	v_pk_add_f32 v[22:23], v[22:23], v[76:77] op_sel_hi:[1,0] neg_lo:[0,1] neg_hi:[0,1]
	v_or_b32_e32 v81, 0, v8
	v_or_b32_e32 v82, 1, v9
	v_min_u32_e32 v80, v81, v82
	v_or_b32_e32 v81, 2, v10
	v_or_b32_e32 v82, 3, v11
	v_min3_u32 v80, v80, v81, v82
	v_or_b32_e32 v81, 4, v12
	v_or_b32_e32 v82, 5, v13
	v_min3_u32 v80, v80, v81, v82
	v_or_b32_e32 v81, 6, v14
	v_or_b32_e32 v82, 7, v15
	v_min3_u32 v80, v80, v81, v82
	v_or_b32_e32 v81, 8, v16
	v_or_b32_e32 v82, 9, v17
	v_min3_u32 v80, v80, v81, v82
	v_or_b32_e32 v81, 10, v18
	v_or_b32_e32 v82, 11, v19
	v_min3_u32 v80, v80, v81, v82
	v_or_b32_e32 v81, 12, v20
	v_or_b32_e32 v82, 13, v21
	v_min3_u32 v80, v80, v81, v82
	v_or_b32_e32 v81, 14, v22
	v_or_b32_e32 v82, 15, v23
	v_min3_u32 v80, v80, v81, v82
	v_pk_mul_f32 v[8:9], v[8:9], s[14:15] op_sel_hi:[1,0]
	v_pk_mul_f32 v[10:11], v[10:11], s[14:15] op_sel_hi:[1,0]
	v_pk_mul_f32 v[12:13], v[12:13], s[14:15] op_sel_hi:[1,0]
	v_pk_mul_f32 v[14:15], v[14:15], s[14:15] op_sel_hi:[1,0]
	v_pk_mul_f32 v[16:17], v[16:17], s[14:15] op_sel_hi:[1,0]
	v_pk_mul_f32 v[18:19], v[18:19], s[14:15] op_sel_hi:[1,0]
	v_pk_mul_f32 v[20:21], v[20:21], s[14:15] op_sel_hi:[1,0]
	v_pk_mul_f32 v[22:23], v[22:23], s[14:15] op_sel_hi:[1,0]
	v_exp_f32_e32 v8, v8
	v_exp_f32_e32 v9, v9
	v_exp_f32_e32 v10, v10
	v_exp_f32_e32 v11, v11
	v_exp_f32_e32 v12, v12
	v_exp_f32_e32 v13, v13
	v_exp_f32_e32 v14, v14
	v_exp_f32_e32 v15, v15
	v_exp_f32_e32 v16, v16
	v_exp_f32_e32 v17, v17
	v_exp_f32_e32 v18, v18
	v_exp_f32_e32 v19, v19
	v_exp_f32_e32 v20, v20
	v_exp_f32_e32 v21, v21
	v_exp_f32_e32 v22, v22
	v_exp_f32_e32 v23, v23
	v_pk_add_f32 v[78:79], v[8:9], v[10:11]
	v_pk_add_f32 v[78:79], v[78:79], v[12:13]
	v_pk_add_f32 v[78:79], v[78:79], v[14:15]
	v_pk_add_f32 v[78:79], v[78:79], v[16:17]
	v_pk_add_f32 v[78:79], v[78:79], v[18:19]
	v_pk_add_f32 v[78:79], v[78:79], v[20:21]
	v_pk_add_f32 v[78:79], v[78:79], v[22:23]
	v_add_f32_e32 v78, v78, v79
	v_cvt_f64_f32_e32 v[86:87], v78
	v_mov_b32_e32 v75, v80
	v_mov_b32_e32 v73, v76
	s_waitcnt vmcnt(33)
	v_max3_f32 v76, v24, v25, v26
	v_max3_f32 v76, v76, v27, v28
	v_max3_f32 v76, v76, v29, v30
	v_max3_f32 v76, v76, v31, v32
	v_max3_f32 v76, v76, v33, v34
	v_max3_f32 v76, v76, v35, v36
	v_max3_f32 v76, v76, v37, v38
	v_max_f32_e32 v76, v76, v39
	v_max_f32_e32 v100, v73, v76
	v_cmp_gt_f32_e64 s[26:27], v76, v73
	v_sub_f32_e32 v83, v73, v100
	v_mul_f32_e32 v83, s14, v83
	v_exp_f32_e32 v83, v83
	v_pk_add_f32 v[24:25], v[24:25], v[100:101] op_sel_hi:[1,0] neg_lo:[0,1] neg_hi:[0,1]
	v_pk_add_f32 v[26:27], v[26:27], v[100:101] op_sel_hi:[1,0] neg_lo:[0,1] neg_hi:[0,1]
	v_pk_add_f32 v[28:29], v[28:29], v[100:101] op_sel_hi:[1,0] neg_lo:[0,1] neg_hi:[0,1]
	v_pk_add_f32 v[30:31], v[30:31], v[100:101] op_sel_hi:[1,0] neg_lo:[0,1] neg_hi:[0,1]
	v_pk_add_f32 v[32:33], v[32:33], v[100:101] op_sel_hi:[1,0] neg_lo:[0,1] neg_hi:[0,1]
	v_pk_add_f32 v[34:35], v[34:35], v[100:101] op_sel_hi:[1,0] neg_lo:[0,1] neg_hi:[0,1]
	v_pk_add_f32 v[36:37], v[36:37], v[100:101] op_sel_hi:[1,0] neg_lo:[0,1] neg_hi:[0,1]
	v_pk_add_f32 v[38:39], v[38:39], v[100:101] op_sel_hi:[1,0] neg_lo:[0,1] neg_hi:[0,1]
	v_cvt_f64_f32_e32 v[90:91], v83
	v_or_b32_e32 v81, 16, v24
	v_or_b32_e32 v82, 17, v25
	v_min_u32_e32 v80, v81, v82
	v_or_b32_e32 v81, 18, v26
	v_or_b32_e32 v82, 19, v27
	v_min3_u32 v80, v80, v81, v82
	v_or_b32_e32 v81, 20, v28
	v_or_b32_e32 v82, 21, v29
	v_min3_u32 v80, v80, v81, v82
	v_or_b32_e32 v81, 22, v30
	v_or_b32_e32 v82, 23, v31
	v_min3_u32 v80, v80, v81, v82
	v_or_b32_e32 v81, 24, v32
	v_or_b32_e32 v82, 25, v33
	v_min3_u32 v80, v80, v81, v82
	v_or_b32_e32 v81, 26, v34
	v_or_b32_e32 v82, 27, v35
	v_min3_u32 v80, v80, v81, v82
	v_or_b32_e32 v81, 28, v36
	v_or_b32_e32 v82, 29, v37
	v_min3_u32 v80, v80, v81, v82
	v_or_b32_e32 v81, 30, v38
	v_or_b32_e32 v82, 31, v39
	v_min3_u32 v80, v80, v81, v82
	v_pk_mul_f32 v[24:25], v[24:25], s[14:15] op_sel_hi:[1,0]
	v_pk_mul_f32 v[26:27], v[26:27], s[14:15] op_sel_hi:[1,0]
	v_pk_mul_f32 v[28:29], v[28:29], s[14:15] op_sel_hi:[1,0]
	v_pk_mul_f32 v[30:31], v[30:31], s[14:15] op_sel_hi:[1,0]
	v_pk_mul_f32 v[32:33], v[32:33], s[14:15] op_sel_hi:[1,0]
	v_pk_mul_f32 v[34:35], v[34:35], s[14:15] op_sel_hi:[1,0]
	v_pk_mul_f32 v[36:37], v[36:37], s[14:15] op_sel_hi:[1,0]
	v_pk_mul_f32 v[38:39], v[38:39], s[14:15] op_sel_hi:[1,0]
	v_exp_f32_e32 v24, v24
	v_exp_f32_e32 v25, v25
	v_exp_f32_e32 v26, v26
	v_exp_f32_e32 v27, v27
	v_exp_f32_e32 v28, v28
	v_exp_f32_e32 v29, v29
	v_exp_f32_e32 v30, v30
	v_exp_f32_e32 v31, v31
	v_exp_f32_e32 v32, v32
	v_exp_f32_e32 v33, v33
	v_exp_f32_e32 v34, v34
	v_exp_f32_e32 v35, v35
	v_exp_f32_e32 v36, v36
	v_exp_f32_e32 v37, v37
	v_exp_f32_e32 v38, v38
	v_exp_f32_e32 v39, v39
	v_pk_add_f32 v[78:79], v[24:25], v[26:27]
	v_pk_add_f32 v[78:79], v[78:79], v[28:29]
	v_pk_add_f32 v[78:79], v[78:79], v[30:31]
	v_pk_add_f32 v[78:79], v[78:79], v[32:33]
	v_pk_add_f32 v[78:79], v[78:79], v[34:35]
	v_pk_add_f32 v[78:79], v[78:79], v[36:37]
	v_pk_add_f32 v[78:79], v[78:79], v[38:39]
	v_add_f32_e32 v78, v78, v79
	v_cvt_f64_f32_e32 v[84:85], v78
	v_cndmask_b32_e64 v75, v75, v80, s[26:27]
	v_mov_b32_e32 v73, v100
	v_fma_f64 v[86:87], v[86:87], v[90:91], v[84:85]
	s_waitcnt vmcnt(17)
	v_max3_f32 v76, v40, v41, v42
	v_max3_f32 v76, v76, v43, v44
	v_max3_f32 v76, v76, v45, v46
	v_max3_f32 v76, v76, v47, v48
	v_max3_f32 v76, v76, v49, v50
	v_max3_f32 v76, v76, v51, v52
	v_max3_f32 v76, v76, v53, v54
	v_max_f32_e32 v76, v76, v55
	v_max_f32_e32 v100, v73, v76
	v_cmp_gt_f32_e64 s[26:27], v76, v73
	v_sub_f32_e32 v83, v73, v100
	v_mul_f32_e32 v83, s14, v83
	v_exp_f32_e32 v83, v83
	v_pk_add_f32 v[40:41], v[40:41], v[100:101] op_sel_hi:[1,0] neg_lo:[0,1] neg_hi:[0,1]
	v_pk_add_f32 v[42:43], v[42:43], v[100:101] op_sel_hi:[1,0] neg_lo:[0,1] neg_hi:[0,1]
	v_pk_add_f32 v[44:45], v[44:45], v[100:101] op_sel_hi:[1,0] neg_lo:[0,1] neg_hi:[0,1]
	v_pk_add_f32 v[46:47], v[46:47], v[100:101] op_sel_hi:[1,0] neg_lo:[0,1] neg_hi:[0,1]
	v_pk_add_f32 v[48:49], v[48:49], v[100:101] op_sel_hi:[1,0] neg_lo:[0,1] neg_hi:[0,1]
	v_pk_add_f32 v[50:51], v[50:51], v[100:101] op_sel_hi:[1,0] neg_lo:[0,1] neg_hi:[0,1]
	v_pk_add_f32 v[52:53], v[52:53], v[100:101] op_sel_hi:[1,0] neg_lo:[0,1] neg_hi:[0,1]
	v_pk_add_f32 v[54:55], v[54:55], v[100:101] op_sel_hi:[1,0] neg_lo:[0,1] neg_hi:[0,1]
	v_cvt_f64_f32_e32 v[90:91], v83
	v_or_b32_e32 v81, 32, v40
	v_or_b32_e32 v82, 33, v41
	v_min_u32_e32 v80, v81, v82
	v_or_b32_e32 v81, 34, v42
	v_or_b32_e32 v82, 35, v43
	v_min3_u32 v80, v80, v81, v82
	v_or_b32_e32 v81, 36, v44
	v_or_b32_e32 v82, 37, v45
	v_min3_u32 v80, v80, v81, v82
	v_or_b32_e32 v81, 38, v46
	v_or_b32_e32 v82, 39, v47
	v_min3_u32 v80, v80, v81, v82
	v_or_b32_e32 v81, 40, v48
	v_or_b32_e32 v82, 41, v49
	v_min3_u32 v80, v80, v81, v82
	v_or_b32_e32 v81, 42, v50
	v_or_b32_e32 v82, 43, v51
	v_min3_u32 v80, v80, v81, v82
	v_or_b32_e32 v81, 44, v52
	v_or_b32_e32 v82, 45, v53
	v_min3_u32 v80, v80, v81, v82
	v_or_b32_e32 v81, 46, v54
	v_or_b32_e32 v82, 47, v55
	v_min3_u32 v80, v80, v81, v82
	v_pk_mul_f32 v[40:41], v[40:41], s[14:15] op_sel_hi:[1,0]
	v_pk_mul_f32 v[42:43], v[42:43], s[14:15] op_sel_hi:[1,0]
	v_pk_mul_f32 v[44:45], v[44:45], s[14:15] op_sel_hi:[1,0]
	v_pk_mul_f32 v[46:47], v[46:47], s[14:15] op_sel_hi:[1,0]
	v_pk_mul_f32 v[48:49], v[48:49], s[14:15] op_sel_hi:[1,0]
	v_pk_mul_f32 v[50:51], v[50:51], s[14:15] op_sel_hi:[1,0]
	v_pk_mul_f32 v[52:53], v[52:53], s[14:15] op_sel_hi:[1,0]
	v_pk_mul_f32 v[54:55], v[54:55], s[14:15] op_sel_hi:[1,0]
	v_exp_f32_e32 v40, v40
	v_exp_f32_e32 v41, v41
	v_exp_f32_e32 v42, v42
	v_exp_f32_e32 v43, v43
	v_exp_f32_e32 v44, v44
	v_exp_f32_e32 v45, v45
	v_exp_f32_e32 v46, v46
	v_exp_f32_e32 v47, v47
	v_exp_f32_e32 v48, v48
	v_exp_f32_e32 v49, v49
	v_exp_f32_e32 v50, v50
	v_exp_f32_e32 v51, v51
	v_exp_f32_e32 v52, v52
	v_exp_f32_e32 v53, v53
	v_exp_f32_e32 v54, v54
	v_exp_f32_e32 v55, v55
	v_pk_add_f32 v[78:79], v[40:41], v[42:43]
	v_pk_add_f32 v[78:79], v[78:79], v[44:45]
	v_pk_add_f32 v[78:79], v[78:79], v[46:47]
	v_pk_add_f32 v[78:79], v[78:79], v[48:49]
	v_pk_add_f32 v[78:79], v[78:79], v[50:51]
	v_pk_add_f32 v[78:79], v[78:79], v[52:53]
	v_pk_add_f32 v[78:79], v[78:79], v[54:55]
	v_add_f32_e32 v78, v78, v79
	v_cvt_f64_f32_e32 v[84:85], v78
	v_cndmask_b32_e64 v75, v75, v80, s[26:27]
	v_mov_b32_e32 v73, v100
	v_fma_f64 v[86:87], v[86:87], v[90:91], v[84:85]
	s_waitcnt vmcnt(9)
	v_max3_f32 v76, v56, v57, v58
	v_max3_f32 v76, v76, v59, v60
	v_max3_f32 v76, v76, v61, v62
	v_max_f32_e32 v76, v76, v63
	v_max_f32_e32 v100, v73, v76
	v_cmp_gt_f32_e64 s[26:27], v76, v73
	v_sub_f32_e32 v83, v73, v100
	v_mul_f32_e32 v83, s14, v83
	v_exp_f32_e32 v83, v83
	v_pk_add_f32 v[56:57], v[56:57], v[100:101] op_sel_hi:[1,0] neg_lo:[0,1] neg_hi:[0,1]
	v_pk_add_f32 v[58:59], v[58:59], v[100:101] op_sel_hi:[1,0] neg_lo:[0,1] neg_hi:[0,1]
	v_pk_add_f32 v[60:61], v[60:61], v[100:101] op_sel_hi:[1,0] neg_lo:[0,1] neg_hi:[0,1]
	v_pk_add_f32 v[62:63], v[62:63], v[100:101] op_sel_hi:[1,0] neg_lo:[0,1] neg_hi:[0,1]
	v_cvt_f64_f32_e32 v[90:91], v83
	v_or_b32_e32 v81, 48, v56
	v_or_b32_e32 v82, 49, v57
	v_min_u32_e32 v80, v81, v82
	v_or_b32_e32 v81, 50, v58
	v_or_b32_e32 v82, 51, v59
	v_min3_u32 v80, v80, v81, v82
	v_or_b32_e32 v81, 52, v60
	v_or_b32_e32 v82, 53, v61
	v_min3_u32 v80, v80, v81, v82
	v_or_b32_e32 v81, 54, v62
	v_or_b32_e32 v82, 55, v63
	v_min3_u32 v80, v80, v81, v82
	v_pk_mul_f32 v[56:57], v[56:57], s[14:15] op_sel_hi:[1,0]
	v_pk_mul_f32 v[58:59], v[58:59], s[14:15] op_sel_hi:[1,0]
	v_pk_mul_f32 v[60:61], v[60:61], s[14:15] op_sel_hi:[1,0]
	v_pk_mul_f32 v[62:63], v[62:63], s[14:15] op_sel_hi:[1,0]
	v_exp_f32_e32 v56, v56
	v_exp_f32_e32 v57, v57
	v_exp_f32_e32 v58, v58
	v_exp_f32_e32 v59, v59
	v_exp_f32_e32 v60, v60
	v_exp_f32_e32 v61, v61
	v_exp_f32_e32 v62, v62
	v_exp_f32_e32 v63, v63
	v_pk_add_f32 v[78:79], v[56:57], v[58:59]
	v_pk_add_f32 v[78:79], v[78:79], v[60:61]
	v_pk_add_f32 v[78:79], v[78:79], v[62:63]
	v_add_f32_e32 v78, v78, v79
	v_cvt_f64_f32_e32 v[84:85], v78
	v_cndmask_b32_e64 v75, v75, v80, s[26:27]
	v_mov_b32_e32 v73, v100
	v_fma_f64 v[86:87], v[86:87], v[90:91], v[84:85]
	s_waitcnt vmcnt(5)
	v_max3_f32 v76, v64, v65, v66
	v_max_f32_e32 v76, v76, v67
	v_max_f32_e32 v100, v73, v76
	v_cmp_gt_f32_e64 s[26:27], v76, v73
	v_sub_f32_e32 v83, v73, v100
	v_mul_f32_e32 v83, s14, v83
	v_exp_f32_e32 v83, v83
	v_pk_add_f32 v[64:65], v[64:65], v[100:101] op_sel_hi:[1,0] neg_lo:[0,1] neg_hi:[0,1]
	v_pk_add_f32 v[66:67], v[66:67], v[100:101] op_sel_hi:[1,0] neg_lo:[0,1] neg_hi:[0,1]
	v_cvt_f64_f32_e32 v[90:91], v83
	v_or_b32_e32 v81, 56, v64
	v_or_b32_e32 v82, 57, v65
	v_min_u32_e32 v80, v81, v82
	v_or_b32_e32 v81, 58, v66
	v_or_b32_e32 v82, 59, v67
	v_min3_u32 v80, v80, v81, v82
	v_pk_mul_f32 v[64:65], v[64:65], s[14:15] op_sel_hi:[1,0]
	v_pk_mul_f32 v[66:67], v[66:67], s[14:15] op_sel_hi:[1,0]
	v_exp_f32_e32 v64, v64
	v_exp_f32_e32 v65, v65
	v_exp_f32_e32 v66, v66
	v_exp_f32_e32 v67, v67
	s_nop 0
	v_pk_add_f32 v[78:79], v[64:65], v[66:67]
	v_add_f32_e32 v78, v78, v79
	v_cvt_f64_f32_e32 v[84:85], v78
	v_cndmask_b32_e64 v75, v75, v80, s[26:27]
	v_mov_b32_e32 v73, v100
	v_fma_f64 v[86:87], v[86:87], v[90:91], v[84:85]
	s_waitcnt vmcnt(0)
	v_max3_f32 v76, v68, v69, v70
	v_max3_f32 v76, v76, v71, v72
	v_max_f32_e32 v100, v73, v76
	v_cmp_gt_f32_e64 s[26:27], v76, v73
	v_sub_f32_e32 v83, v73, v100
	v_mul_f32_e32 v83, s14, v83
	v_exp_f32_e32 v83, v83
	v_pk_add_f32 v[68:69], v[68:69], v[100:101] op_sel_hi:[1,0] neg_lo:[0,1] neg_hi:[0,1]
	v_pk_add_f32 v[70:71], v[70:71], v[100:101] op_sel_hi:[1,0] neg_lo:[0,1] neg_hi:[0,1]
	v_sub_f32_e32 v72, v72, v100
	v_cvt_f64_f32_e32 v[90:91], v83
	v_or_b32_e32 v81, 60, v68
	v_or_b32_e32 v82, 61, v69
	v_min_u32_e32 v80, v81, v82
	v_or_b32_e32 v81, 62, v70
	v_or_b32_e32 v82, 63, v71
	v_min3_u32 v80, v80, v81, v82
	v_or_b32_e32 v81, 64, v72
	v_min_u32_e32 v80, v80, v81
	v_pk_mul_f32 v[68:69], v[68:69], s[14:15] op_sel_hi:[1,0]
	v_pk_mul_f32 v[70:71], v[70:71], s[14:15] op_sel_hi:[1,0]
	v_mul_f32_e32 v72, s14, v72
	v_exp_f32_e32 v68, v68
	v_exp_f32_e32 v69, v69
	v_exp_f32_e32 v70, v70
	v_exp_f32_e32 v71, v71
	v_exp_f32_e32 v72, v72
	v_cndmask_b32_e64 v75, v75, v80, s[26:27]
	v_pk_add_f32 v[78:79], v[68:69], v[70:71]
	v_add_f32_e32 v78, v78, v79
	v_add_f32_e32 v78, v78, v72
	v_cvt_f64_f32_e32 v[84:85], v78
	v_fma_f64 v[86:87], v[86:87], v[90:91], v[84:85]
	v_rcp_f64_e32 v[88:89], v[86:87]
	v_cmp_gt_u32_e32 vcc, 64, v75
	s_and_b64 vcc, vcc, s[36:37]
	v_fma_f64 v[90:91], -v[86:87], v[88:89], 1.0
	v_fma_f64 v[88:89], v[90:91], v[88:89], v[88:89]
	v_cvt_f32_f64_e32 v3, v[88:89]
	v_cndmask_b32_e32 v74, 0, v3, vcc
	global_store_dwordx2 v98, v[74:75], s[6:7]
